# GEMM3 routing epilogue: 112 more canonicalising copies removed by reading the source register directly
# speedup vs baseline: 1.0027x; 1.0011x over previous
; #define PG8_LAS __attribute__((address_space(3)))
; #define CE(a, b) do { const float hi_ = fmaxf(a, b), lo_ = fminf(a, b); a = hi_; b = lo_; } while (0)
; __device__ __forceinline__ void merge_top16(float (&v)[16], const float (&nw)[16]) {
;     v[0] = fmaxf(v[0], nw[15]); v[1] = fmaxf(v[1], nw[14]); v[2] = fmaxf(v[2], nw[13]); v[3] = fmaxf(v[3], nw[12]); v[4] = fmaxf(v[4], nw[11]); v[5] = fmaxf(v[5], nw[10]); v[6] = fmaxf(v[6], nw[9]); v[7] = fmaxf(v[7], nw[8]); v[8] = fmaxf(v[8], nw[7]); v[9] = fmaxf(v[9], nw[6]); v[10] = fmaxf(v[10], nw[5]); v[11] = fmaxf(v[11], nw[4]); v[12] = fmaxf(v[12], nw[3]); v[13] = fmaxf(v[13], nw[2]); v[14] = fmaxf(v[14], nw[1]); v[15] = fmaxf(v[15], nw[0]);
;     CE(v[0], v[8]); CE(v[1], v[9]); CE(v[2], v[10]); CE(v[3], v[11]);
;     CE(v[4], v[12]); CE(v[5], v[13]); CE(v[6], v[14]); CE(v[7], v[15]);
;     CE(v[0], v[4]); CE(v[1], v[5]); CE(v[2], v[6]); CE(v[3], v[7]);
;     CE(v[8], v[12]); CE(v[9], v[13]); CE(v[10], v[14]); CE(v[11], v[15]);
;     CE(v[0], v[2]); CE(v[1], v[3]); CE(v[4], v[6]); CE(v[5], v[7]);
;     CE(v[8], v[10]); CE(v[9], v[11]); CE(v[12], v[14]); CE(v[13], v[15]);
;     CE(v[0], v[1]); CE(v[2], v[3]); CE(v[4], v[5]); CE(v[6], v[7]);
;     CE(v[8], v[9]); CE(v[10], v[11]); CE(v[12], v[13]); CE(v[14], v[15]);
; }
;     __device__ __forceinline__ void fused(f32x4 (&acc)[2][2][4][2], const Unit& u, int wr, int wc, int fr, int fq, PG8_LAS unsigned char* lds, int wid, int lane) const {
;     ...
;             if (half == 0) {
;                 float nw[16];
; #pragma unroll
;                 for (int i = 0; i < 4; ++i) { const f32x4 v = *(const PG8_LAS f32x4*)(tile + row * 16 + 4 * i); nw[4 * i] = v[0]; nw[4 * i + 1] = v[1]; nw[4 * i + 2] = v[2]; nw[4 * i + 3] = v[3]; }
;                 merge_top16(run, nw);
.LBB0_582:
	s_waitcnt lgkmcnt(0)
	s_barrier
	s_cmp_lt_u32 s51, 4
	s_cselect_b64 s[20:21], -1, 0
	s_cmp_gt_u32 s51, 3
	s_cbranch_scc1 .LBB0_584
	ds_read_b128 v[106:109], v97 offset:48
	ds_read_b128 v[110:113], v97 offset:32
	ds_read_b128 v[114:117], v97
	ds_read_b128 v[130:133], v97 offset:16
	s_waitcnt lgkmcnt(0)
	v_max_f32_e32 v76, v76, v109
	v_max_f32_e32 v77, v77, v108
	v_max_f32_e32 v78, v78, v107
	v_max_f32_e32 v79, v79, v106
	v_max_f32_e32 v72, v72, v113
	v_max_f32_e32 v73, v73, v112
	v_max_f32_e32 v74, v74, v111
	v_max_f32_e32 v75, v75, v110
	v_max_f32_e32 v68, v68, v133
	v_max_f32_e32 v69, v69, v132
	v_max_f32_e32 v70, v70, v131
	v_max_f32_e32 v71, v71, v130
	v_max_f32_e32 v64, v64, v117
	v_max_f32_e32 v65, v65, v116
	v_max_f32_e32 v66, v66, v115
	v_max_f32_e32 v67, v67, v114
	v_max_f32_e32 v105, v76, v68
	v_min_f32_e32 v68, v76, v68
	v_max_f32_e32 v76, v77, v69
	v_min_f32_e32 v69, v77, v69
	v_max_f32_e32 v77, v78, v70
	v_min_f32_e32 v70, v78, v70
	v_max_f32_e32 v78, v79, v71
	v_min_f32_e32 v71, v79, v71
	v_max_f32_e32 v79, v72, v64
	v_min_f32_e32 v64, v72, v64
	v_max_f32_e32 v72, v73, v65
	v_min_f32_e32 v65, v73, v65
	v_max_f32_e32 v73, v74, v66
	v_min_f32_e32 v66, v74, v66
	v_max_f32_e32 v74, v75, v67
	v_min_f32_e32 v67, v75, v67
	v_max_f32_e32 v75, v105, v79
	v_min_f32_e32 v79, v105, v79
	v_max_f32_e32 v105, v76, v72
	v_min_f32_e32 v72, v76, v72
	v_max_f32_e32 v76, v77, v73
	v_min_f32_e32 v73, v77, v73
	v_max_f32_e32 v77, v78, v74
	v_min_f32_e32 v74, v78, v74
	v_max_f32_e32 v78, v68, v64
	v_min_f32_e32 v64, v68, v64
	v_max_f32_e32 v68, v69, v65
	v_min_f32_e32 v65, v69, v65
	v_max_f32_e32 v69, v70, v66
	v_min_f32_e32 v66, v70, v66
	v_max_f32_e32 v70, v71, v67
	v_min_f32_e32 v67, v71, v67
	v_max_f32_e32 v71, v75, v76
	v_min_f32_e32 v75, v75, v76
	v_max_f32_e32 v106, v105, v77
	v_min_f32_e32 v105, v105, v77
	v_max_f32_e32 v107, v79, v73
	v_min_f32_e32 v108, v79, v73
	v_max_f32_e32 v73, v72, v74
	v_min_f32_e32 v109, v72, v74
	v_max_f32_e32 v110, v78, v69
	v_min_f32_e32 v111, v78, v69
	v_max_f32_e32 v69, v68, v70
	v_min_f32_e32 v112, v68, v70
	v_max_f32_e32 v113, v64, v66
	v_min_f32_e32 v114, v64, v66
	v_max_f32_e32 v66, v65, v67
	v_min_f32_e32 v67, v65, v67
	v_max_f32_e32 v76, v71, v106
	v_min_f32_e32 v77, v71, v106
	v_max_f32_e32 v78, v75, v105
	v_min_f32_e32 v79, v75, v105
	v_max_f32_e32 v72, v107, v73
	v_min_f32_e32 v73, v107, v73
	v_max_f32_e32 v74, v108, v109
	v_min_f32_e32 v75, v108, v109
	v_max_f32_e32 v68, v110, v69
	v_min_f32_e32 v69, v110, v69
	v_max_f32_e32 v70, v111, v112
	v_min_f32_e32 v71, v111, v112
	v_max_f32_e32 v64, v113, v66
	v_min_f32_e32 v65, v113, v66
	v_max_f32_e32 v66, v114, v67
	v_min_f32_e32 v67, v114, v67

; #define PG8_LAS __attribute__((address_space(3)))
; #define CE(a, b) do { const float hi_ = fmaxf(a, b), lo_ = fminf(a, b); a = hi_; b = lo_; } while (0)
; __device__ __forceinline__ void merge_top16(float (&v)[16], const float (&nw)[16]) {
;     v[0] = fmaxf(v[0], nw[15]); v[1] = fmaxf(v[1], nw[14]); v[2] = fmaxf(v[2], nw[13]); v[3] = fmaxf(v[3], nw[12]); v[4] = fmaxf(v[4], nw[11]); v[5] = fmaxf(v[5], nw[10]); v[6] = fmaxf(v[6], nw[9]); v[7] = fmaxf(v[7], nw[8]); v[8] = fmaxf(v[8], nw[7]); v[9] = fmaxf(v[9], nw[6]); v[10] = fmaxf(v[10], nw[5]); v[11] = fmaxf(v[11], nw[4]); v[12] = fmaxf(v[12], nw[3]); v[13] = fmaxf(v[13], nw[2]); v[14] = fmaxf(v[14], nw[1]); v[15] = fmaxf(v[15], nw[0]);
;     CE(v[0], v[8]); CE(v[1], v[9]); CE(v[2], v[10]); CE(v[3], v[11]);
;     CE(v[4], v[12]); CE(v[5], v[13]); CE(v[6], v[14]); CE(v[7], v[15]);
;     CE(v[0], v[4]); CE(v[1], v[5]); CE(v[2], v[6]); CE(v[3], v[7]);
;     CE(v[8], v[12]); CE(v[9], v[13]); CE(v[10], v[14]); CE(v[11], v[15]);
;     CE(v[0], v[2]); CE(v[1], v[3]); CE(v[4], v[6]); CE(v[5], v[7]);
;     CE(v[8], v[10]); CE(v[9], v[11]); CE(v[12], v[14]); CE(v[13], v[15]);
;     CE(v[0], v[1]); CE(v[2], v[3]); CE(v[4], v[5]); CE(v[6], v[7]);
;     CE(v[8], v[9]); CE(v[10], v[11]); CE(v[12], v[13]); CE(v[14], v[15]);
; }
;     __device__ __forceinline__ void fused(f32x4 (&acc)[2][2][4][2], const Unit& u, int wr, int wc, int fr, int fq, PG8_LAS unsigned char* lds, int wid, int lane) const {
;     ...
;             if (half == 0) {
;                 float nw[16];
; #pragma unroll
;                 for (int i = 0; i < 4; ++i) { const f32x4 v = *(const PG8_LAS f32x4*)(tile + row * 16 + 4 * i); nw[4 * i] = v[0]; nw[4 * i + 1] = v[1]; nw[4 * i + 2] = v[2]; nw[4 * i + 3] = v[3]; }
;                 merge_top16(run, nw);
.LBB0_586:
	s_waitcnt lgkmcnt(0)
	s_barrier
	v_cndmask_b32_e64 v16, 0, 1, s[20:21]
	v_cmp_ne_u32_e64 s[4:5], 1, v16
	s_andn2_b64 vcc, exec, s[20:21]
	s_cbranch_vccnz .LBB0_588
	ds_read_b128 v[16:19], v97 offset:48
	ds_read_b128 v[20:23], v97 offset:32
	ds_read_b128 v[24:27], v97
	ds_read_b128 v[28:31], v97 offset:16
	s_waitcnt lgkmcnt(0)
	v_max_f32_e32 v15, v15, v16
	v_max_f32_e32 v8, v8, v23
	v_max_f32_e32 v9, v9, v22
	v_max_f32_e32 v10, v10, v21
	v_max_f32_e32 v11, v11, v20
	v_max_f32_e32 v4, v4, v31
	v_max_f32_e32 v5, v5, v30
	v_max_f32_e32 v6, v6, v29
	v_max_f32_e32 v7, v7, v28
	v_max_f32_e32 v0, v0, v27
	v_max_f32_e32 v1, v1, v26
	v_max_f32_e32 v2, v2, v25
	v_max_f32_e32 v12, v12, v19
	v_max_f32_e32 v13, v13, v18
	v_max_f32_e32 v14, v14, v17
	v_max_f32_e32 v3, v3, v24
	v_max_f32_e32 v16, v12, v4
	v_min_f32_e32 v4, v12, v4
	v_max_f32_e32 v12, v13, v5
	v_min_f32_e32 v5, v13, v5
	v_max_f32_e32 v13, v14, v6
	v_min_f32_e32 v6, v14, v6
	v_max_f32_e32 v14, v15, v7
	v_min_f32_e32 v7, v15, v7
	v_max_f32_e32 v15, v8, v0
	v_min_f32_e32 v0, v8, v0
	v_max_f32_e32 v8, v9, v1
	v_min_f32_e32 v1, v9, v1
	v_max_f32_e32 v9, v10, v2
	v_min_f32_e32 v2, v10, v2
	v_max_f32_e32 v10, v11, v3
	v_min_f32_e32 v3, v11, v3
	v_max_f32_e32 v11, v16, v15
	v_min_f32_e32 v15, v16, v15
	v_max_f32_e32 v16, v12, v8
	v_min_f32_e32 v8, v12, v8
	v_max_f32_e32 v12, v13, v9
	v_min_f32_e32 v9, v13, v9
	v_max_f32_e32 v13, v14, v10
	v_min_f32_e32 v10, v14, v10
	v_max_f32_e32 v14, v4, v0
	v_min_f32_e32 v0, v4, v0
	v_max_f32_e32 v4, v5, v1
	v_min_f32_e32 v1, v5, v1
	v_max_f32_e32 v5, v6, v2
	v_min_f32_e32 v2, v6, v2
	v_max_f32_e32 v6, v7, v3
	v_min_f32_e32 v3, v7, v3
	v_max_f32_e32 v7, v11, v12
	v_min_f32_e32 v11, v11, v12
	v_max_f32_e32 v17, v16, v13
	v_min_f32_e32 v16, v16, v13
	v_max_f32_e32 v18, v15, v9
	v_min_f32_e32 v19, v15, v9
	v_max_f32_e32 v9, v8, v10
	v_min_f32_e32 v20, v8, v10
	v_max_f32_e32 v21, v14, v5
	v_min_f32_e32 v22, v14, v5
	v_max_f32_e32 v5, v4, v6
	v_min_f32_e32 v23, v4, v6
	v_max_f32_e32 v24, v0, v2
	v_min_f32_e32 v25, v0, v2
	v_max_f32_e32 v2, v1, v3
	v_min_f32_e32 v3, v1, v3
	v_max_f32_e32 v12, v7, v17
	v_min_f32_e32 v13, v7, v17
	v_max_f32_e32 v14, v11, v16
	v_min_f32_e32 v15, v11, v16
	v_max_f32_e32 v8, v18, v9
	v_min_f32_e32 v9, v18, v9
	v_max_f32_e32 v10, v19, v20
	v_min_f32_e32 v11, v19, v20
	v_max_f32_e32 v4, v21, v5
	v_min_f32_e32 v5, v21, v5
	v_max_f32_e32 v6, v22, v23
	v_min_f32_e32 v7, v22, v23
	v_max_f32_e32 v0, v24, v2
	v_min_f32_e32 v1, v24, v2
	v_max_f32_e32 v2, v25, v3
	v_min_f32_e32 v3, v25, v3

; #define PG8_LAS __attribute__((address_space(3)))
; #define CE(a, b) do { const float hi_ = fmaxf(a, b), lo_ = fminf(a, b); a = hi_; b = lo_; } while (0)
; __device__ __forceinline__ void merge_top16(float (&v)[16], const float (&nw)[16]) {
;     v[0] = fmaxf(v[0], nw[15]); v[1] = fmaxf(v[1], nw[14]); v[2] = fmaxf(v[2], nw[13]); v[3] = fmaxf(v[3], nw[12]); v[4] = fmaxf(v[4], nw[11]); v[5] = fmaxf(v[5], nw[10]); v[6] = fmaxf(v[6], nw[9]); v[7] = fmaxf(v[7], nw[8]); v[8] = fmaxf(v[8], nw[7]); v[9] = fmaxf(v[9], nw[6]); v[10] = fmaxf(v[10], nw[5]); v[11] = fmaxf(v[11], nw[4]); v[12] = fmaxf(v[12], nw[3]); v[13] = fmaxf(v[13], nw[2]); v[14] = fmaxf(v[14], nw[1]); v[15] = fmaxf(v[15], nw[0]);
;     CE(v[0], v[8]); CE(v[1], v[9]); CE(v[2], v[10]); CE(v[3], v[11]);
;     CE(v[4], v[12]); CE(v[5], v[13]); CE(v[6], v[14]); CE(v[7], v[15]);
;     CE(v[0], v[4]); CE(v[1], v[5]); CE(v[2], v[6]); CE(v[3], v[7]);
;     CE(v[8], v[12]); CE(v[9], v[13]); CE(v[10], v[14]); CE(v[11], v[15]);
;     CE(v[0], v[2]); CE(v[1], v[3]); CE(v[4], v[6]); CE(v[5], v[7]);
;     CE(v[8], v[10]); CE(v[9], v[11]); CE(v[12], v[14]); CE(v[13], v[15]);
;     CE(v[0], v[1]); CE(v[2], v[3]); CE(v[4], v[5]); CE(v[6], v[7]);
;     CE(v[8], v[9]); CE(v[10], v[11]); CE(v[12], v[13]); CE(v[14], v[15]);
; }
;     __device__ __forceinline__ void fused(f32x4 (&acc)[2][2][4][2], const Unit& u, int wr, int wc, int fr, int fq, PG8_LAS unsigned char* lds, int wid, int lane) const {
;     ...
;             if (half == 0) {
;                 float nw[16];
; #pragma unroll
;                 for (int i = 0; i < 4; ++i) { const f32x4 v = *(const PG8_LAS f32x4*)(tile + row * 16 + 4 * i); nw[4 * i] = v[0]; nw[4 * i + 1] = v[1]; nw[4 * i + 2] = v[2]; nw[4 * i + 3] = v[3]; }
;                 merge_top16(run, nw);
.LBB0_600:
	s_waitcnt lgkmcnt(0)
	s_barrier
	s_cmp_lt_u32 s44, 4
	s_cselect_b64 s[14:15], -1, 0
	s_cmp_gt_u32 s44, 3
	s_cbranch_scc1 .LBB0_602
	ds_read_b128 v[106:109], v97 offset:48
	ds_read_b128 v[110:113], v97 offset:32
	ds_read_b128 v[114:117], v97
	ds_read_b128 v[130:133], v97 offset:16
	s_waitcnt lgkmcnt(0)
	v_max_f32_e32 v76, v76, v109
	v_max_f32_e32 v77, v77, v108
	v_max_f32_e32 v78, v78, v107
	v_max_f32_e32 v79, v79, v106
	v_max_f32_e32 v72, v72, v113
	v_max_f32_e32 v73, v73, v112
	v_max_f32_e32 v74, v74, v111
	v_max_f32_e32 v75, v75, v110
	v_max_f32_e32 v68, v68, v133
	v_max_f32_e32 v69, v69, v132
	v_max_f32_e32 v70, v70, v131
	v_max_f32_e32 v71, v71, v130
	v_max_f32_e32 v64, v64, v117
	v_max_f32_e32 v65, v65, v116
	v_max_f32_e32 v66, v66, v115
	v_max_f32_e32 v67, v67, v114
	v_max_f32_e32 v105, v76, v68
	v_min_f32_e32 v68, v76, v68
	v_max_f32_e32 v76, v77, v69
	v_min_f32_e32 v69, v77, v69
	v_max_f32_e32 v77, v78, v70
	v_min_f32_e32 v70, v78, v70
	v_max_f32_e32 v78, v79, v71
	v_min_f32_e32 v71, v79, v71
	v_max_f32_e32 v79, v72, v64
	v_min_f32_e32 v64, v72, v64
	v_max_f32_e32 v72, v73, v65
	v_min_f32_e32 v65, v73, v65
	v_max_f32_e32 v73, v74, v66
	v_min_f32_e32 v66, v74, v66
	v_max_f32_e32 v74, v75, v67
	v_min_f32_e32 v67, v75, v67
	v_max_f32_e32 v75, v105, v79
	v_min_f32_e32 v79, v105, v79
	v_max_f32_e32 v105, v76, v72
	v_min_f32_e32 v72, v76, v72
	v_max_f32_e32 v76, v77, v73
	v_min_f32_e32 v73, v77, v73
	v_max_f32_e32 v77, v78, v74
	v_min_f32_e32 v74, v78, v74
	v_max_f32_e32 v78, v68, v64
	v_min_f32_e32 v64, v68, v64
	v_max_f32_e32 v68, v69, v65
	v_min_f32_e32 v65, v69, v65
	v_max_f32_e32 v69, v70, v66
	v_min_f32_e32 v66, v70, v66
	v_max_f32_e32 v70, v71, v67
	v_min_f32_e32 v67, v71, v67
	v_max_f32_e32 v71, v75, v76
	v_min_f32_e32 v75, v75, v76
	v_max_f32_e32 v106, v105, v77
	v_min_f32_e32 v105, v105, v77
	v_max_f32_e32 v107, v79, v73
	v_min_f32_e32 v108, v79, v73
	v_max_f32_e32 v73, v72, v74
	v_min_f32_e32 v109, v72, v74
	v_max_f32_e32 v110, v78, v69
	v_min_f32_e32 v111, v78, v69
	v_max_f32_e32 v69, v68, v70
	v_min_f32_e32 v112, v68, v70
	v_max_f32_e32 v113, v64, v66
	v_min_f32_e32 v114, v64, v66
	v_max_f32_e32 v66, v65, v67
	v_min_f32_e32 v67, v65, v67
	v_max_f32_e32 v76, v71, v106
	v_min_f32_e32 v77, v71, v106
	v_max_f32_e32 v78, v75, v105
	v_min_f32_e32 v79, v75, v105
	v_max_f32_e32 v72, v107, v73
	v_min_f32_e32 v73, v107, v73
	v_max_f32_e32 v74, v108, v109
	v_min_f32_e32 v75, v108, v109
	v_max_f32_e32 v68, v110, v69
	v_min_f32_e32 v69, v110, v69
	v_max_f32_e32 v70, v111, v112
	v_min_f32_e32 v71, v111, v112
	v_max_f32_e32 v64, v113, v66
	v_min_f32_e32 v65, v113, v66
	v_max_f32_e32 v66, v114, v67
	v_min_f32_e32 v67, v114, v67

; #define PG8_LAS __attribute__((address_space(3)))
; #define CE(a, b) do { const float hi_ = fmaxf(a, b), lo_ = fminf(a, b); a = hi_; b = lo_; } while (0)
; __device__ __forceinline__ void merge_top16(float (&v)[16], const float (&nw)[16]) {
;     v[0] = fmaxf(v[0], nw[15]); v[1] = fmaxf(v[1], nw[14]); v[2] = fmaxf(v[2], nw[13]); v[3] = fmaxf(v[3], nw[12]); v[4] = fmaxf(v[4], nw[11]); v[5] = fmaxf(v[5], nw[10]); v[6] = fmaxf(v[6], nw[9]); v[7] = fmaxf(v[7], nw[8]); v[8] = fmaxf(v[8], nw[7]); v[9] = fmaxf(v[9], nw[6]); v[10] = fmaxf(v[10], nw[5]); v[11] = fmaxf(v[11], nw[4]); v[12] = fmaxf(v[12], nw[3]); v[13] = fmaxf(v[13], nw[2]); v[14] = fmaxf(v[14], nw[1]); v[15] = fmaxf(v[15], nw[0]);
;     CE(v[0], v[8]); CE(v[1], v[9]); CE(v[2], v[10]); CE(v[3], v[11]);
;     CE(v[4], v[12]); CE(v[5], v[13]); CE(v[6], v[14]); CE(v[7], v[15]);
;     CE(v[0], v[4]); CE(v[1], v[5]); CE(v[2], v[6]); CE(v[3], v[7]);
;     CE(v[8], v[12]); CE(v[9], v[13]); CE(v[10], v[14]); CE(v[11], v[15]);
;     CE(v[0], v[2]); CE(v[1], v[3]); CE(v[4], v[6]); CE(v[5], v[7]);
;     CE(v[8], v[10]); CE(v[9], v[11]); CE(v[12], v[14]); CE(v[13], v[15]);
;     CE(v[0], v[1]); CE(v[2], v[3]); CE(v[4], v[5]); CE(v[6], v[7]);
;     CE(v[8], v[9]); CE(v[10], v[11]); CE(v[12], v[13]); CE(v[14], v[15]);
; }
;     __device__ __forceinline__ void fused(f32x4 (&acc)[2][2][4][2], const Unit& u, int wr, int wc, int fr, int fq, PG8_LAS unsigned char* lds, int wid, int lane) const {
;     ...
;             if (half == 0) {
;                 float nw[16];
; #pragma unroll
;                 for (int i = 0; i < 4; ++i) { const f32x4 v = *(const PG8_LAS f32x4*)(tile + row * 16 + 4 * i); nw[4 * i] = v[0]; nw[4 * i + 1] = v[1]; nw[4 * i + 2] = v[2]; nw[4 * i + 3] = v[3]; }
;                 merge_top16(run, nw);
.LBB0_604:
	s_waitcnt lgkmcnt(0)
	s_barrier
	v_cndmask_b32_e64 v16, 0, 1, s[14:15]
	v_cmp_ne_u32_e64 s[4:5], 1, v16
	s_andn2_b64 vcc, exec, s[14:15]
	s_cbranch_vccnz .LBB0_606
	ds_read_b128 v[16:19], v97 offset:48
	ds_read_b128 v[20:23], v97 offset:32
	ds_read_b128 v[24:27], v97
	ds_read_b128 v[28:31], v97 offset:16
	s_waitcnt lgkmcnt(0)
	v_max_f32_e32 v15, v15, v16
	v_max_f32_e32 v8, v8, v23
	v_max_f32_e32 v9, v9, v22
	v_max_f32_e32 v10, v10, v21
	v_max_f32_e32 v11, v11, v20
	v_max_f32_e32 v4, v4, v31
	v_max_f32_e32 v5, v5, v30
	v_max_f32_e32 v6, v6, v29
	v_max_f32_e32 v7, v7, v28
	v_max_f32_e32 v0, v0, v27
	v_max_f32_e32 v1, v1, v26
	v_max_f32_e32 v2, v2, v25
	v_max_f32_e32 v12, v12, v19
	v_max_f32_e32 v13, v13, v18
	v_max_f32_e32 v14, v14, v17
	v_max_f32_e32 v3, v3, v24
	v_max_f32_e32 v16, v12, v4
	v_min_f32_e32 v4, v12, v4
	v_max_f32_e32 v12, v13, v5
	v_min_f32_e32 v5, v13, v5
	v_max_f32_e32 v13, v14, v6
	v_min_f32_e32 v6, v14, v6
	v_max_f32_e32 v14, v15, v7
	v_min_f32_e32 v7, v15, v7
	v_max_f32_e32 v15, v8, v0
	v_min_f32_e32 v0, v8, v0
	v_max_f32_e32 v8, v9, v1
	v_min_f32_e32 v1, v9, v1
	v_max_f32_e32 v9, v10, v2
	v_min_f32_e32 v2, v10, v2
	v_max_f32_e32 v10, v11, v3
	v_min_f32_e32 v3, v11, v3
	v_max_f32_e32 v11, v16, v15
	v_min_f32_e32 v15, v16, v15
	v_max_f32_e32 v16, v12, v8
	v_min_f32_e32 v8, v12, v8
	v_max_f32_e32 v12, v13, v9
	v_min_f32_e32 v9, v13, v9
	v_max_f32_e32 v13, v14, v10
	v_min_f32_e32 v10, v14, v10
	v_max_f32_e32 v14, v4, v0
	v_min_f32_e32 v0, v4, v0
	v_max_f32_e32 v4, v5, v1
	v_min_f32_e32 v1, v5, v1
	v_max_f32_e32 v5, v6, v2
	v_min_f32_e32 v2, v6, v2
	v_max_f32_e32 v6, v7, v3
	v_min_f32_e32 v3, v7, v3
	v_max_f32_e32 v7, v11, v12
	v_min_f32_e32 v11, v11, v12
	v_max_f32_e32 v17, v16, v13
	v_min_f32_e32 v16, v16, v13
	v_max_f32_e32 v18, v15, v9
	v_min_f32_e32 v19, v15, v9
	v_max_f32_e32 v9, v8, v10
	v_min_f32_e32 v20, v8, v10
	v_max_f32_e32 v21, v14, v5
	v_min_f32_e32 v22, v14, v5
	v_max_f32_e32 v5, v4, v6
	v_min_f32_e32 v23, v4, v6
	v_max_f32_e32 v24, v0, v2
	v_min_f32_e32 v25, v0, v2
	v_max_f32_e32 v2, v1, v3
	v_min_f32_e32 v3, v1, v3
	v_max_f32_e32 v12, v7, v17
	v_min_f32_e32 v13, v7, v17
	v_max_f32_e32 v14, v11, v16
	v_min_f32_e32 v15, v11, v16
	v_max_f32_e32 v8, v18, v9
	v_min_f32_e32 v9, v18, v9
	v_max_f32_e32 v10, v19, v20
	v_min_f32_e32 v11, v19, v20
	v_max_f32_e32 v4, v21, v5
	v_min_f32_e32 v5, v21, v5
	v_max_f32_e32 v6, v22, v23
	v_min_f32_e32 v7, v22, v23
	v_max_f32_e32 v0, v24, v2
	v_min_f32_e32 v1, v24, v2
	v_max_f32_e32 v2, v25, v3
	v_min_f32_e32 v3, v25, v3
